# speedup vs baseline: 1.0058x; 1.0058x over previous
.LBB2_37:
	s_waitcnt lgkmcnt(0)
	v_mfma_f32_32x32x16_f16 v[102:117], v[122:125], v[98:101], 0
	v_exp_f32_e32 v4, v38
	v_exp_f32_e32 v5, v40
	v_exp_f32_e32 v238, v43
	v_exp_f32_e32 v239, v45
	v_mfma_f32_32x32x16_f16 v[102:117], v[126:129], v[154:157], v[102:117]
	v_exp_f32_e32 v154, v39
	v_exp_f32_e32 v155, v41
	v_exp_f32_e32 v156, v42
	v_exp_f32_e32 v157, v44
	v_cvt_pk_f16_f32 v38, v4, v154
	v_cvt_pk_f16_f32 v39, v5, v155
	v_cvt_pk_f16_f32 v40, v156, v238
	v_cvt_pk_f16_f32 v41, v157, v239
	v_mfma_f32_32x32x16_f16 v[102:117], v[130:133], v[90:93], v[102:117]
	v_exp_f32_e32 v240, v46
	v_exp_f32_e32 v242, v47
	v_exp_f32_e32 v241, v48
	v_exp_f32_e32 v243, v49
	v_exp_f32_e32 v244, v50
	v_exp_f32_e32 v246, v51
	v_exp_f32_e32 v245, v52
	v_exp_f32_e32 v247, v53
	v_cvt_pk_f16_f32 v42, v240, v242
	v_cvt_pk_f16_f32 v43, v241, v243
	v_cvt_pk_f16_f32 v44, v244, v246
	v_cvt_pk_f16_f32 v45, v245, v247
	v_mfma_f32_32x32x16_f16 v[102:117], v[134:137], v[94:97], v[102:117]
	v_mfma_f32_32x32x16_f16 v[86:101], v[122:125], v[86:89], 0
	v_exp_f32_e32 v248, v58
	v_exp_f32_e32 v250, v59
	v_exp_f32_e32 v249, v60
	v_exp_f32_e32 v251, v61
	v_mfma_f32_32x32x16_f16 v[86:101], v[126:129], v[150:153], v[86:101]
	v_exp_f32_e32 v150, v54
	v_exp_f32_e32 v152, v55
	v_exp_f32_e32 v151, v56
	v_exp_f32_e32 v153, v57
	v_cvt_pk_f16_f32 v56, v248, v250
	v_cvt_pk_f16_f32 v54, v150, v152
	v_cvt_pk_f16_f32 v57, v249, v251
	v_cvt_pk_f16_f32 v55, v151, v153
	v_mfma_f32_32x32x16_f16 v[86:101], v[130:133], v[142:145], v[86:101]
	ds_read_b128 v[46:49], v235 offset:16384
	ds_read_b128 v[50:53], v235 offset:20480
	ds_read_b128 v[58:61], v236 offset:16384
	ds_read_b128 v[142:145], v236 offset:20480
	v_exp_f32_e32 v236, v67
	v_exp_f32_e32 v67, v68
	v_exp_f32_e32 v237, v69
	v_pk_add_f32 v[4:5], v[4:5], 0 op_sel_hi:[1,0]
	v_pk_add_f32 v[68:69], v[154:155], 0 op_sel_hi:[1,0]
	v_pk_add_f32 v[4:5], v[156:157], v[4:5]
	v_pk_add_f32 v[68:69], v[238:239], v[68:69]
	v_mfma_f32_32x32x16_f16 v[86:101], v[134:137], v[146:149], v[86:101]
	v_exp_f32_e32 v146, v62
	v_exp_f32_e32 v148, v63
	v_exp_f32_e32 v147, v64
	v_exp_f32_e32 v149, v65
	v_pk_add_f32 v[4:5], v[240:241], v[4:5]
	v_pk_add_f32 v[68:69], v[242:243], v[68:69]
	v_exp_f32_e32 v66, v66
	v_pk_add_f32 v[4:5], v[244:245], v[4:5]
	v_pk_add_f32 v[68:69], v[246:247], v[68:69]
	v_pk_add_f32 v[4:5], v[150:151], v[4:5]
	v_pk_add_f32 v[68:69], v[152:153], v[68:69]
	v_pk_add_f32 v[4:5], v[248:249], v[4:5]
	v_pk_add_f32 v[68:69], v[250:251], v[68:69]
	v_pk_add_f32 v[4:5], v[146:147], v[4:5]
	v_pk_add_f32 v[68:69], v[148:149], v[68:69]
	v_pk_add_f32 v[4:5], v[66:67], v[4:5]
	v_pk_add_f32 v[68:69], v[236:237], v[68:69]
	v_cvt_pk_f16_f32 v62, v146, v148
	v_pk_add_f32 v[4:5], v[4:5], v[68:69]
	v_cvt_pk_f16_f32 v63, v147, v149
	v_add_f32_e32 v2, v4, v5
	v_cvt_pk_f16_f32 v64, v66, v236
	v_cvt_pk_f16_f32 v65, v67, v237
	v_add_f32_e32 v164, v164, v2
	s_waitcnt lgkmcnt(0)
	v_mfma_f32_32x32x16_f16 v[22:37], v[46:49], v[38:41], v[22:37]
	v_cndmask_b32_e64 v2, v70, v102, s[52:53]
	v_cndmask_b32_e64 v4, v71, v103, s[4:5]
	ds_read_b128 v[66:69], v233 offset:16384
	ds_read_b128 v[146:149], v233 offset:20480
	ds_read_b128 v[150:153], v234 offset:16384
	ds_read_b128 v[154:157], v234 offset:20480
	ds_write2_b32 v181, v2, v4 offset1:32
	v_cndmask_b32_e64 v2, v72, v104, s[6:7]
	v_cndmask_b32_e64 v4, v73, v105, s[8:9]
	ds_write2_b32 v181, v2, v4 offset0:64 offset1:96
	v_mfma_f32_32x32x16_f16 v[6:21], v[50:53], v[38:41], v[6:21]
	v_cndmask_b32_e64 v2, v74, v106, s[10:11]
	v_cndmask_b32_e64 v4, v75, v107, s[12:13]
	v_add_u32_e32 v5, 0x400, v181
	ds_write2_b32 v5, v2, v4 offset1:32
	v_cndmask_b32_e64 v2, v76, v108, s[14:15]
	v_cndmask_b32_e64 v4, v77, v109, s[16:17]
	ds_write2_b32 v5, v2, v4 offset0:64 offset1:96
	v_cndmask_b32_e64 v2, v78, v110, s[18:19]
	v_cndmask_b32_e64 v4, v79, v111, s[20:21]
	v_add_u32_e32 v233, 0x800, v181
	ds_write2_b32 v233, v2, v4 offset1:32
	v_cndmask_b32_e64 v2, v80, v112, s[22:23]
	v_cndmask_b32_e64 v4, v81, v113, s[24:25]
	ds_write2_b32 v233, v2, v4 offset0:64 offset1:96
	v_cndmask_b32_e64 v2, v82, v114, s[26:27]
	v_cndmask_b32_e64 v4, v83, v115, s[28:29]
	v_add_u32_e32 v234, 0xc00, v181
	ds_write2_b32 v234, v2, v4 offset1:32
	v_cndmask_b32_e64 v2, v84, v116, s[30:31]
	v_cndmask_b32_e64 v4, v85, v117, s[34:35]
	ds_write2_b32 v234, v2, v4 offset0:64 offset1:96
	v_mfma_f32_32x32x16_f16 v[22:37], v[58:61], v[42:45], v[22:37]
	v_mfma_f32_32x32x16_f16 v[6:21], v[142:145], v[42:45], v[6:21]
	s_waitcnt lgkmcnt(8)
	ds_read_b32 v38, v214
	ds_read_b32 v39, v215
	ds_read_b32 v40, v216
	ds_read_b32 v41, v217
	ds_read_b32 v42, v218
	ds_read_b32 v43, v219
	ds_read_b32 v44, v220
	ds_read_b32 v45, v221
	ds_read_b32 v46, v222
	ds_read_b32 v47, v223
	ds_read_b32 v48, v224
	ds_read_b32 v49, v225
	ds_read_b32 v50, v226
	ds_read_b32 v51, v227
	ds_read_b32 v52, v228
	ds_read_b32 v53, v229
	v_mfma_f32_32x32x16_f16 v[22:37], v[66:69], v[54:57], v[22:37]
	v_cndmask_b32_e64 v2, v102, v86, s[52:53]
	v_cndmask_b32_e64 v4, v103, v87, s[4:5]
	ds_write2_b32 v181, v2, v4 offset1:32
	v_cndmask_b32_e64 v2, v104, v88, s[6:7]
	v_cndmask_b32_e64 v4, v105, v89, s[8:9]
	ds_write2_b32 v181, v2, v4 offset0:64 offset1:96
	v_cndmask_b32_e64 v2, v106, v90, s[10:11]
	v_mfma_f32_32x32x16_f16 v[6:21], v[146:149], v[54:57], v[6:21]
	v_cndmask_b32_e64 v4, v107, v91, s[12:13]
	ds_write2_b32 v5, v2, v4 offset1:32
	v_cndmask_b32_e64 v2, v108, v92, s[14:15]
	v_cndmask_b32_e64 v4, v109, v93, s[16:17]
	ds_write2_b32 v5, v2, v4 offset0:64 offset1:96
	v_cndmask_b32_e64 v2, v110, v94, s[18:19]
	v_cndmask_b32_e64 v4, v111, v95, s[20:21]
	ds_write2_b32 v233, v2, v4 offset1:32
	v_cndmask_b32_e64 v2, v112, v96, s[22:23]
	v_cndmask_b32_e64 v4, v113, v97, s[24:25]
	ds_write2_b32 v233, v2, v4 offset0:64 offset1:96
	v_cndmask_b32_e64 v2, v114, v98, s[26:27]
	v_cndmask_b32_e64 v4, v115, v99, s[28:29]
	ds_write2_b32 v234, v2, v4 offset1:32
	v_cndmask_b32_e64 v2, v116, v100, s[30:31]
	v_cndmask_b32_e64 v4, v117, v101, s[34:35]
	ds_write2_b32 v234, v2, v4 offset0:64 offset1:96
	v_mfma_f32_32x32x16_f16 v[22:37], v[150:153], v[62:65], v[22:37]
	v_mfma_f32_32x32x16_f16 v[6:21], v[154:157], v[62:65], v[6:21]
	ds_read_b32 v54, v214
	ds_read_b32 v55, v215
	ds_read_b32 v56, v216
	ds_read_b32 v57, v217
	ds_read_b32 v58, v218
	ds_read_b32 v59, v219
	ds_read_b32 v60, v220
	ds_read_b32 v61, v221
	ds_read_b32 v62, v222
	ds_read_b32 v63, v223
	ds_read_b32 v64, v224
	ds_read_b32 v65, v225
	ds_read_b32 v66, v226
	ds_read_b32 v67, v227
	ds_read_b32 v68, v228
	ds_read_b32 v69, v229

.LBB2_51:
	s_waitcnt lgkmcnt(0)
	v_mfma_f32_32x32x16_f16 v[102:117], v[122:125], v[82:85], 0
	v_exp_f32_e32 v4, v38
	v_exp_f32_e32 v5, v40
	v_exp_f32_e32 v238, v43
	v_exp_f32_e32 v239, v45
	v_mfma_f32_32x32x16_f16 v[102:117], v[126:129], v[154:157], v[102:117]
	v_exp_f32_e32 v154, v39
	v_exp_f32_e32 v155, v41
	v_exp_f32_e32 v156, v42
	v_exp_f32_e32 v157, v44
	v_cvt_pk_f16_f32 v38, v4, v154
	v_cvt_pk_f16_f32 v39, v5, v155
	v_cvt_pk_f16_f32 v40, v156, v238
	v_cvt_pk_f16_f32 v41, v157, v239
	v_mfma_f32_32x32x16_f16 v[102:117], v[130:133], v[74:77], v[102:117]
	v_exp_f32_e32 v240, v46
	v_exp_f32_e32 v242, v47
	v_exp_f32_e32 v241, v48
	v_exp_f32_e32 v243, v49
	v_exp_f32_e32 v244, v50
	v_exp_f32_e32 v246, v51
	v_exp_f32_e32 v245, v52
	v_exp_f32_e32 v247, v53
	v_cvt_pk_f16_f32 v42, v240, v242
	v_cvt_pk_f16_f32 v43, v241, v243
	v_cvt_pk_f16_f32 v44, v244, v246
	v_cvt_pk_f16_f32 v45, v245, v247
	v_mfma_f32_32x32x16_f16 v[102:117], v[134:137], v[78:81], v[102:117]
	v_mfma_f32_32x32x16_f16 v[70:85], v[122:125], v[70:73], 0
	v_exp_f32_e32 v248, v58
	v_exp_f32_e32 v250, v59
	v_exp_f32_e32 v249, v60
	v_exp_f32_e32 v251, v61
	v_mfma_f32_32x32x16_f16 v[70:85], v[126:129], v[150:153], v[70:85]
	v_exp_f32_e32 v150, v54
	v_exp_f32_e32 v152, v55
	v_exp_f32_e32 v151, v56
	v_exp_f32_e32 v153, v57
	v_cvt_pk_f16_f32 v56, v248, v250
	v_cvt_pk_f16_f32 v54, v150, v152
	v_cvt_pk_f16_f32 v57, v249, v251
	v_cvt_pk_f16_f32 v55, v151, v153
	v_mfma_f32_32x32x16_f16 v[70:85], v[130:133], v[142:145], v[70:85]
	ds_read_b128 v[46:49], v235 offset:24576
	ds_read_b128 v[50:53], v235 offset:28672
	ds_read_b128 v[58:61], v236 offset:24576
	ds_read_b128 v[142:145], v236 offset:28672
	v_exp_f32_e32 v236, v67
	v_exp_f32_e32 v67, v68
	v_exp_f32_e32 v237, v69
	v_pk_add_f32 v[4:5], v[4:5], 0 op_sel_hi:[1,0]
	v_pk_add_f32 v[68:69], v[154:155], 0 op_sel_hi:[1,0]
	v_pk_add_f32 v[4:5], v[156:157], v[4:5]
	v_pk_add_f32 v[68:69], v[238:239], v[68:69]
	v_mfma_f32_32x32x16_f16 v[70:85], v[134:137], v[146:149], v[70:85]
	v_exp_f32_e32 v146, v62
	v_exp_f32_e32 v148, v63
	v_exp_f32_e32 v147, v64
	v_exp_f32_e32 v149, v65
	v_pk_add_f32 v[4:5], v[240:241], v[4:5]
	v_pk_add_f32 v[68:69], v[242:243], v[68:69]
	v_exp_f32_e32 v66, v66
	v_pk_add_f32 v[4:5], v[244:245], v[4:5]
	v_pk_add_f32 v[68:69], v[246:247], v[68:69]
	v_pk_add_f32 v[4:5], v[150:151], v[4:5]
	v_pk_add_f32 v[68:69], v[152:153], v[68:69]
	v_pk_add_f32 v[4:5], v[248:249], v[4:5]
	v_pk_add_f32 v[68:69], v[250:251], v[68:69]
	v_pk_add_f32 v[4:5], v[146:147], v[4:5]
	v_pk_add_f32 v[68:69], v[148:149], v[68:69]
	v_pk_add_f32 v[4:5], v[66:67], v[4:5]
	v_pk_add_f32 v[68:69], v[236:237], v[68:69]
	v_cvt_pk_f16_f32 v62, v146, v148
	v_pk_add_f32 v[4:5], v[4:5], v[68:69]
	v_cvt_pk_f16_f32 v63, v147, v149
	v_add_f32_e32 v2, v4, v5
	v_cvt_pk_f16_f32 v64, v66, v236
	v_cvt_pk_f16_f32 v65, v67, v237
	v_add_f32_e32 v164, v164, v2
	s_waitcnt lgkmcnt(0)
	v_mfma_f32_32x32x16_f16 v[22:37], v[46:49], v[38:41], v[22:37]
	v_cndmask_b32_e64 v2, v86, v102, s[52:53]
	v_cndmask_b32_e64 v4, v87, v103, s[4:5]
	ds_read_b128 v[66:69], v233 offset:24576
	ds_read_b128 v[146:149], v233 offset:28672
	ds_read_b128 v[150:153], v234 offset:24576
	ds_read_b128 v[154:157], v234 offset:28672
	ds_write2_b32 v181, v2, v4 offset1:32
	v_cndmask_b32_e64 v2, v88, v104, s[6:7]
	v_cndmask_b32_e64 v4, v89, v105, s[8:9]
	ds_write2_b32 v181, v2, v4 offset0:64 offset1:96
	v_mfma_f32_32x32x16_f16 v[6:21], v[50:53], v[38:41], v[6:21]
	v_cndmask_b32_e64 v2, v90, v106, s[10:11]
	v_cndmask_b32_e64 v4, v91, v107, s[12:13]
	v_add_u32_e32 v5, 0x400, v181
	ds_write2_b32 v5, v2, v4 offset1:32
	v_cndmask_b32_e64 v2, v92, v108, s[14:15]
	v_cndmask_b32_e64 v4, v93, v109, s[16:17]
	ds_write2_b32 v5, v2, v4 offset0:64 offset1:96
	v_cndmask_b32_e64 v2, v94, v110, s[18:19]
	v_cndmask_b32_e64 v4, v95, v111, s[20:21]
	v_add_u32_e32 v233, 0x800, v181
	ds_write2_b32 v233, v2, v4 offset1:32
	v_cndmask_b32_e64 v2, v96, v112, s[22:23]
	v_cndmask_b32_e64 v4, v97, v113, s[24:25]
	ds_write2_b32 v233, v2, v4 offset0:64 offset1:96
	v_cndmask_b32_e64 v2, v98, v114, s[26:27]
	v_cndmask_b32_e64 v4, v99, v115, s[28:29]
	v_add_u32_e32 v234, 0xc00, v181
	ds_write2_b32 v234, v2, v4 offset1:32
	v_cndmask_b32_e64 v2, v100, v116, s[30:31]
	v_cndmask_b32_e64 v4, v101, v117, s[34:35]
	ds_write2_b32 v234, v2, v4 offset0:64 offset1:96
	v_mfma_f32_32x32x16_f16 v[22:37], v[58:61], v[42:45], v[22:37]
	v_mfma_f32_32x32x16_f16 v[6:21], v[142:145], v[42:45], v[6:21]
	s_waitcnt lgkmcnt(8)
	ds_read_b32 v38, v214
	ds_read_b32 v39, v215
	ds_read_b32 v40, v216
	ds_read_b32 v41, v217
	ds_read_b32 v42, v218
	ds_read_b32 v43, v219
	ds_read_b32 v44, v220
	ds_read_b32 v45, v221
	ds_read_b32 v46, v222
	ds_read_b32 v47, v223
	ds_read_b32 v48, v224
	ds_read_b32 v49, v225
	ds_read_b32 v50, v226
	ds_read_b32 v51, v227
	ds_read_b32 v52, v228
	ds_read_b32 v53, v229
	v_mfma_f32_32x32x16_f16 v[22:37], v[66:69], v[54:57], v[22:37]
	v_cndmask_b32_e64 v2, v102, v70, s[52:53]
	v_cndmask_b32_e64 v4, v103, v71, s[4:5]
	ds_write2_b32 v181, v2, v4 offset1:32
	v_cndmask_b32_e64 v2, v104, v72, s[6:7]
	v_cndmask_b32_e64 v4, v105, v73, s[8:9]
	ds_write2_b32 v181, v2, v4 offset0:64 offset1:96
	v_cndmask_b32_e64 v2, v106, v74, s[10:11]
	v_mfma_f32_32x32x16_f16 v[6:21], v[146:149], v[54:57], v[6:21]
	v_cndmask_b32_e64 v4, v107, v75, s[12:13]
	ds_write2_b32 v5, v2, v4 offset1:32
	v_cndmask_b32_e64 v2, v108, v76, s[14:15]
	v_cndmask_b32_e64 v4, v109, v77, s[16:17]
	ds_write2_b32 v5, v2, v4 offset0:64 offset1:96
	v_cndmask_b32_e64 v2, v110, v78, s[18:19]
	v_cndmask_b32_e64 v4, v111, v79, s[20:21]
	ds_write2_b32 v233, v2, v4 offset1:32
	v_cndmask_b32_e64 v2, v112, v80, s[22:23]
	v_cndmask_b32_e64 v4, v113, v81, s[24:25]
	ds_write2_b32 v233, v2, v4 offset0:64 offset1:96
	v_cndmask_b32_e64 v2, v114, v82, s[26:27]
	v_cndmask_b32_e64 v4, v115, v83, s[28:29]
	ds_write2_b32 v234, v2, v4 offset1:32
	v_cndmask_b32_e64 v2, v116, v84, s[30:31]
	v_cndmask_b32_e64 v4, v117, v85, s[34:35]
	ds_write2_b32 v234, v2, v4 offset0:64 offset1:96
	v_mfma_f32_32x32x16_f16 v[22:37], v[150:153], v[62:65], v[22:37]
	v_mfma_f32_32x32x16_f16 v[6:21], v[154:157], v[62:65], v[6:21]
	ds_read_b32 v54, v214
	ds_read_b32 v55, v215
	ds_read_b32 v56, v216
	ds_read_b32 v57, v217
	ds_read_b32 v58, v218
	ds_read_b32 v59, v219
	ds_read_b32 v60, v220
	ds_read_b32 v61, v221
	ds_read_b32 v62, v222
	ds_read_b32 v63, v223
	ds_read_b32 v64, v224
	ds_read_b32 v65, v225
	ds_read_b32 v66, v226
	ds_read_b32 v67, v227
	ds_read_b32 v68, v228
	ds_read_b32 v69, v229
